# attention softmax (MLA x2, SWA): 24 identity v_max x,x,x removed, 33 canonicalizing copies folded into their v_max consumer (~5 fewer VALU per half-step)
# speedup vs baseline: 1.0116x; 1.0014x over previous
; #define VMW() asm volatile("s_waitcnt vmcnt(0)" ::: "memory")
; #define SWRITE_H(bf) do { SWRITE_HV(bf); SWRITE_HK(bf); } while (0)
; template <int MODE>
; __device__ __forceinline__ void partialSM(f32x16& p0, f32x16& p1, float& m_reg, float& mn, float& alpha) {
;     constexpr float SCALE = Cfg<MODE>::SCALE;
;     float pmax = p0[0];
; #pragma unroll
;     for (int r = 1; r < 16; ++r) pmax = fmaxf(pmax, p0[r]);
; #pragma unroll
;     for (int r = 0; r < 16; ++r) pmax = fmaxf(pmax, p1[r]);
;     { auto rr = __builtin_amdgcn_permlane32_swap(__float_as_uint(pmax), __float_as_uint(pmax), false, false);
;       pmax = fmaxf(__uint_as_float(rr[0]), __uint_as_float(rr[1])); }
;     constexpr float C2 = 1.4426950408889634f * SCALE;
;     if (__builtin_expect(__all((pmax - m_reg) * SCALE <= THR), 1)) { mn = m_reg; alpha = 1.f; }
;     else { mn = fmaxf(m_reg, pmax); alpha = __builtin_amdgcn_exp2f((m_reg - mn) * C2); m_reg = mn; }
; template <int MODE>
; __device__ __forceinline__ void attn_block_pipe(const BlockRef& cur, const BlockRef& nxt, char* lds, LAS unsigned char* ldsl, Seam<MODE>& S) {
;     ...
;     MASKT(pA0, pA1, 0, 0); partialSM<MODE>(pA0, pA1, m_reg, mnA, alA);
;     if (NT > 1) { VMW(); SWRITE_H(1); }
.LBB0_519:
	s_nop 9
	v_max_f32_e32 v38, v20, v21
	v_max3_f32 v38, v38, v22, v23
	v_max3_f32 v38, v38, v24, v25
	v_max3_f32 v38, v38, v26, v27
	v_max3_f32 v38, v38, v28, v29
	v_max3_f32 v38, v38, v30, v31
	v_max3_f32 v38, v38, v32, v33
	v_max3_f32 v38, v38, v34, v35
	v_max3_f32 v38, v38, v4, v5
	v_max3_f32 v38, v38, v6, v7
	v_max3_f32 v38, v38, v8, v9
	v_max3_f32 v38, v38, v10, v11
	v_max3_f32 v38, v38, v12, v13
	v_max3_f32 v38, v38, v14, v15
	v_max3_f32 v38, v38, v16, v17
	v_max3_f32 v38, v38, v18, v19
	v_mov_b32_e32 v39, v38
	s_nop 1
	v_permlane32_swap_b32_e32 v38, v39
	v_max_f32_e32 v38, v38, v39
	v_add_f32_e32 v39, 0x7149f2ca, v38
	v_mul_f32_e32 v39, 0x3d93cd3a, v39
	v_cmp_ge_f32_e32 vcc, s66, v39
	s_cmp_eq_u64 vcc, exec
	s_cselect_b64 s[4:5], -1, 0
	s_andn2_b64 vcc, exec, s[50:51]
	s_cbranch_vccnz .LBB0_521
	s_waitcnt vmcnt(0)
	s_waitcnt vmcnt(0)
	ds_write_b128 v2, v[114:117] offset:16384
	ds_write_b128 v2, v[118:121] offset:24576

; template <int MODE>
; __device__ __forceinline__ void partialSM(f32x16& p0, f32x16& p1, float& m_reg, float& mn, float& alpha) {
;     constexpr float SCALE = Cfg<MODE>::SCALE;
;     float pmax = p0[0];
; #pragma unroll
;     for (int r = 1; r < 16; ++r) pmax = fmaxf(pmax, p0[r]);
; #pragma unroll
;     for (int r = 0; r < 16; ++r) pmax = fmaxf(pmax, p1[r]);
;     { auto rr = __builtin_amdgcn_permlane32_swap(__float_as_uint(pmax), __float_as_uint(pmax), false, false);
;       pmax = fmaxf(__uint_as_float(rr[0]), __uint_as_float(rr[1])); }
;     constexpr float C2 = 1.4426950408889634f * SCALE;
;     if (__builtin_expect(__all((pmax - m_reg) * SCALE <= THR), 1)) { mn = m_reg; alpha = 1.f; }
;     else { mn = fmaxf(m_reg, pmax); alpha = __builtin_amdgcn_exp2f((m_reg - mn) * C2); m_reg = mn; }
.LBB0_527:
	v_max_f32_e32 v12, v102, v103
	v_max3_f32 v12, v12, v104, v105
	v_max3_f32 v12, v12, v106, v107
	v_max3_f32 v12, v12, v108, v109
	v_max3_f32 v12, v12, v110, v111
	v_max3_f32 v12, v12, v112, v113
	v_max3_f32 v12, v12, v114, v115
	v_max3_f32 v12, v12, v116, v117
	v_max3_f32 v12, v12, v86, v87
	v_max3_f32 v12, v12, v88, v89
	v_max3_f32 v12, v12, v90, v91
	v_max3_f32 v12, v12, v92, v93
	v_max3_f32 v12, v12, v94, v95
	v_max3_f32 v12, v12, v96, v97
	v_max3_f32 v12, v12, v98, v99
	v_max3_f32 v12, v12, v100, v101
	v_mov_b32_e32 v13, v12
	s_nop 1
	v_permlane32_swap_b32_e32 v12, v13
	v_max_f32_e32 v12, v12, v13
	v_sub_f32_e32 v13, v12, v178
	v_max_f32_e32 v12, v178, v12
	v_sub_f32_e32 v14, v178, v12
	v_mul_f32_e32 v14, 0x3dd53b94, v14
	v_mul_f32_e32 v13, 0x3d93cd3a, v13
	v_exp_f32_e32 v14, v14
	v_cmp_ge_f32_e32 vcc, s66, v13
	s_cmp_eq_u64 vcc, exec
	s_cselect_b64 s[6:7], -1, 0
	s_waitcnt vmcnt(0) lgkmcnt(0)
	s_barrier
	s_waitcnt vmcnt(0)
	v_cndmask_b32_e64 v227, v14, 1.0, s[6:7]
	v_cmp_gt_f32_e32 vcc, 1.0, v227
	ds_write_b128 v2, v[4:7]
	ds_write_b128 v2, v[8:11] offset:8192
	s_cbranch_vccz .LBB0_531
	s_and_saveexec_b64 s[50:51], s[4:5]
	ds_write_b32 v209, v227 offset:128
	s_or_b64 exec, exec, s[50:51]
	s_waitcnt lgkmcnt(0)
	ds_read_b128 v[82:85], v208 offset:224
	ds_read_b128 v[118:121], v208 offset:192
	ds_read_b128 v[122:125], v208 offset:160
	ds_read_b128 v[126:129], v208 offset:128
	s_waitcnt lgkmcnt(3)
	v_pk_mul_f32 v[80:81], v[80:81], v[84:85]
	s_waitcnt lgkmcnt(2)
	v_pk_mul_f32 v[76:77], v[76:77], v[120:121]
	s_waitcnt lgkmcnt(1)
	v_pk_mul_f32 v[72:73], v[72:73], v[124:125]
	s_waitcnt lgkmcnt(0)
	v_pk_mul_f32 v[68:69], v[68:69], v[128:129]
	v_pk_mul_f32 v[78:79], v[78:79], v[82:83]
	v_pk_mul_f32 v[74:75], v[74:75], v[118:119]
	v_pk_mul_f32 v[70:71], v[70:71], v[122:123]
	v_pk_mul_f32 v[66:67], v[66:67], v[126:127]
	v_pk_mul_f32 v[64:65], v[64:65], v[84:85]
	v_pk_mul_f32 v[60:61], v[60:61], v[120:121]
	v_pk_mul_f32 v[56:57], v[56:57], v[124:125]
	v_pk_mul_f32 v[52:53], v[52:53], v[128:129]
	v_pk_mul_f32 v[62:63], v[62:63], v[82:83]
	v_pk_mul_f32 v[58:59], v[58:59], v[118:119]
	v_pk_mul_f32 v[54:55], v[54:55], v[122:123]
	v_pk_mul_f32 v[50:51], v[50:51], v[126:127]
	v_pk_mul_f32 v[48:49], v[48:49], v[84:85]
	v_pk_mul_f32 v[44:45], v[44:45], v[120:121]
	v_pk_mul_f32 v[40:41], v[40:41], v[124:125]
	v_pk_mul_f32 v[36:37], v[36:37], v[128:129]
	v_pk_mul_f32 v[46:47], v[46:47], v[82:83]
	v_pk_mul_f32 v[42:43], v[42:43], v[118:119]
	v_pk_mul_f32 v[38:39], v[38:39], v[122:123]
	v_pk_mul_f32 v[34:35], v[34:35], v[126:127]
	v_pk_mul_f32 v[32:33], v[32:33], v[84:85]
	v_pk_mul_f32 v[28:29], v[28:29], v[120:121]
	v_pk_mul_f32 v[24:25], v[24:25], v[124:125]
	v_pk_mul_f32 v[20:21], v[20:21], v[128:129]
	v_pk_mul_f32 v[30:31], v[30:31], v[82:83]
	v_pk_mul_f32 v[26:27], v[26:27], v[118:119]
	v_pk_mul_f32 v[22:23], v[22:23], v[122:123]
	v_pk_mul_f32 v[18:19], v[18:19], v[126:127]

; template <int MODE>
; __device__ __forceinline__ void partialSM(f32x16& p0, f32x16& p1, float& m_reg, float& mn, float& alpha) {
;     constexpr float SCALE = Cfg<MODE>::SCALE;
;     float pmax = p0[0];
; #pragma unroll
;     for (int r = 1; r < 16; ++r) pmax = fmaxf(pmax, p0[r]);
; #pragma unroll
;     for (int r = 0; r < 16; ++r) pmax = fmaxf(pmax, p1[r]);
;     { auto rr = __builtin_amdgcn_permlane32_swap(__float_as_uint(pmax), __float_as_uint(pmax), false, false);
;       pmax = fmaxf(__uint_as_float(rr[0]), __uint_as_float(rr[1])); }
;     constexpr float C2 = 1.4426950408889634f * SCALE;
;     if (__builtin_expect(__all((pmax - m_reg) * SCALE <= THR), 1)) { mn = m_reg; alpha = 1.f; }
;     else { mn = fmaxf(m_reg, pmax); alpha = __builtin_amdgcn_exp2f((m_reg - mn) * C2); m_reg = mn; }
.LBB0_535:
	v_max_f32_e32 v12, v130, v131
	v_max3_f32 v12, v12, v132, v133
	v_max3_f32 v12, v12, v134, v135
	v_max3_f32 v12, v12, v136, v137
	v_max3_f32 v12, v12, v138, v139
	v_max3_f32 v12, v12, v140, v141
	v_max3_f32 v12, v12, v142, v143
	v_max3_f32 v12, v12, v144, v145
	v_max3_f32 v12, v12, v114, v115
	v_max3_f32 v12, v12, v116, v117
	v_max3_f32 v12, v12, v118, v119
	v_max3_f32 v12, v12, v120, v121
	v_max3_f32 v12, v12, v122, v123
	v_max3_f32 v12, v12, v124, v125
	v_max3_f32 v12, v12, v126, v127
	v_max3_f32 v12, v12, v128, v129
	v_mov_b32_e32 v13, v12
	s_nop 1
	v_permlane32_swap_b32_e32 v12, v13
	v_max_f32_e32 v12, v12, v13
	v_sub_f32_e32 v13, v12, v228
	v_mul_f32_e32 v13, 0x3d93cd3a, v13
	v_cmp_ge_f32_e32 vcc, s66, v13
	s_cmp_eq_u64 vcc, exec
	s_cselect_b64 s[6:7], -1, 0
	s_andn2_b64 vcc, exec, s[50:51]
	s_waitcnt vmcnt(0) lgkmcnt(0)
	s_barrier
	s_cbranch_vccnz .LBB0_537
	s_waitcnt vmcnt(0)
	ds_write_b128 v2, v[4:7] offset:16384
	ds_write_b128 v2, v[8:11] offset:24576
.LBB0_537:
	v_max_f32_e32 v5, v228, v12
	v_sub_f32_e32 v4, v228, v5
	v_mul_f32_e32 v4, 0x3dd53b94, v4
	v_exp_f32_e32 v4, v4
	s_nop 0
	v_cndmask_b32_e64 v4, v4, 1.0, s[6:7]
	v_cmp_gt_f32_e32 vcc, 1.0, v4
	s_cbranch_vccz .LBB0_524
	s_and_saveexec_b64 s[50:51], s[4:5]
	s_cbranch_execz .LBB0_523
	ds_write_b32 v209, v4 offset:128
	s_branch .LBB0_523

; #define RESC(a) do { if (__any((a) < 1.f)) { if (hi == 0) al_l[r32] = (a); asm volatile("s_waitcnt lgkmcnt(0)" ::: "memory");              \
;                      _Pragma("unroll") for (int d_ = 0; d_ < 4; ++d_) _Pragma("unroll") for (int r = 0; r < 16; ++r) o[d_][r] *= al_l[crow(r, hi)]; } } while (0)
; #define RESC(a) do { if (__any((a) < 1.f)) { if (hi == 0) al_l[r32] = (a); asm volatile("s_waitcnt lgkmcnt(0)" ::: "memory");              \
;                      _Pragma("unroll") for (int d_ = 0; d_ < 4; ++d_) _Pragma("unroll") for (int r = 0; r < 16; ++r) o[d_][r] *= al_l[crow(r, hi)]; } } while (0)
; #define RESC(a) do { if (__any((a) < 1.f)) { if (hi == 0) al_l[r32] = (a); asm volatile("s_waitcnt lgkmcnt(0)" ::: "memory");              \
;                      _Pragma("unroll") for (int d_ = 0; d_ < 4; ++d_) _Pragma("unroll") for (int r = 0; r < 16; ++r) o[d_][r] *= al_l[crow(r, hi)]; } } while (0)
; template <int MODE>
; __device__ __forceinline__ void partialSM(f32x16& p0, f32x16& p1, float& m_reg, float& mn, float& alpha) {
;     constexpr float SCALE = Cfg<MODE>::SCALE;
;     float pmax = p0[0];
; #pragma unroll
;     for (int r = 1; r < 16; ++r) pmax = fmaxf(pmax, p0[r]);
; #pragma unroll
;     for (int r = 0; r < 16; ++r) pmax = fmaxf(pmax, p1[r]);
;     { auto rr = __builtin_amdgcn_permlane32_swap(__float_as_uint(pmax), __float_as_uint(pmax), false, false);
;       pmax = fmaxf(__uint_as_float(rr[0]), __uint_as_float(rr[1])); }
;     constexpr float C2 = 1.4426950408889634f * SCALE;
;     if (__builtin_expect(__all((pmax - m_reg) * SCALE <= THR), 1)) { mn = m_reg; alpha = 1.f; }
;     else { mn = fmaxf(m_reg, pmax); alpha = __builtin_amdgcn_exp2f((m_reg - mn) * C2); m_reg = mn; }
; template <int MODE>
; __device__ __forceinline__ void attn_block_pipe(const BlockRef& cur, const BlockRef& nxt, char* lds, LAS unsigned char* ldsl, Seam<MODE>& S) {
;     ...
;     if (even) { MASKT(pB0, pB1, NT - 1, 1); partialSM<MODE>(pB0, pB1, m_reg, mnB, alB); __syncthreads(); RESC(alB);
.LBB0_546:
	v_max_f32_e32 v16, v82, v83
	v_max3_f32 v16, v16, v84, v85
	v_max3_f32 v16, v16, v86, v87
	v_max3_f32 v16, v16, v88, v89
	v_max3_f32 v16, v16, v90, v91
	v_max3_f32 v16, v16, v92, v93
	v_max3_f32 v16, v16, v94, v95
	v_max3_f32 v16, v16, v96, v97
	v_max3_f32 v16, v16, v98, v99
	v_max3_f32 v16, v16, v100, v101
	v_max3_f32 v16, v16, v102, v103
	v_max3_f32 v16, v16, v104, v105
	v_max3_f32 v16, v16, v106, v107
	v_max3_f32 v16, v16, v108, v109
	v_max3_f32 v16, v16, v110, v111
	v_max3_f32 v16, v16, v112, v113
	v_mov_b32_e32 v17, v16
	s_nop 1
	v_permlane32_swap_b32_e32 v16, v17
	v_max_f32_e32 v16, v16, v17
	v_sub_f32_e32 v17, v16, v178
	v_mul_f32_e32 v126, 0x3d93cd3a, v17
	v_max_f32_e32 v17, v178, v16
	v_sub_f32_e32 v16, v178, v17
	v_mul_f32_e32 v16, 0x3dd53b94, v16
	v_exp_f32_e32 v16, v16
	v_cmp_ge_f32_e32 vcc, s66, v126
	s_cmp_eq_u64 vcc, exec
	s_cselect_b64 s[4:5], -1, 0
	v_cndmask_b32_e64 v16, v16, 1.0, s[4:5]
	v_cmp_gt_f32_e32 vcc, 1.0, v16
	s_waitcnt vmcnt(0) lgkmcnt(0)
	s_barrier
	s_cbranch_vccz .LBB0_550
	v_cmp_gt_u32_e32 vcc, 32, v207
	s_and_saveexec_b64 s[6:7], vcc
	ds_write_b32 v209, v16 offset:128
	s_or_b64 exec, exec, s[6:7]
	s_waitcnt lgkmcnt(0)
	ds_read_b128 v[126:129], v208 offset:224
	ds_read_b128 v[130:133], v208 offset:192
	ds_read_b128 v[134:137], v208 offset:160
	ds_read_b128 v[138:141], v208 offset:128
	s_waitcnt lgkmcnt(3)
	v_pk_mul_f32 v[80:81], v[80:81], v[128:129]
	s_waitcnt lgkmcnt(2)
	v_pk_mul_f32 v[76:77], v[76:77], v[132:133]
	s_waitcnt lgkmcnt(1)
	v_pk_mul_f32 v[72:73], v[72:73], v[136:137]
	s_waitcnt lgkmcnt(0)
	v_pk_mul_f32 v[68:69], v[68:69], v[140:141]
	v_pk_mul_f32 v[78:79], v[78:79], v[126:127]
	v_pk_mul_f32 v[74:75], v[74:75], v[130:131]
	v_pk_mul_f32 v[70:71], v[70:71], v[134:135]
	v_pk_mul_f32 v[66:67], v[66:67], v[138:139]
	v_pk_mul_f32 v[64:65], v[64:65], v[128:129]
	v_pk_mul_f32 v[60:61], v[60:61], v[132:133]
	v_pk_mul_f32 v[56:57], v[56:57], v[136:137]
	v_pk_mul_f32 v[52:53], v[52:53], v[140:141]
	v_pk_mul_f32 v[62:63], v[62:63], v[126:127]
	v_pk_mul_f32 v[58:59], v[58:59], v[130:131]
	v_pk_mul_f32 v[54:55], v[54:55], v[134:135]
	v_pk_mul_f32 v[50:51], v[50:51], v[138:139]
	v_pk_mul_f32 v[48:49], v[48:49], v[128:129]
	v_pk_mul_f32 v[44:45], v[44:45], v[132:133]
	v_pk_mul_f32 v[40:41], v[40:41], v[136:137]
	v_pk_mul_f32 v[36:37], v[36:37], v[140:141]
	v_pk_mul_f32 v[46:47], v[46:47], v[126:127]
	v_pk_mul_f32 v[42:43], v[42:43], v[130:131]
	v_pk_mul_f32 v[38:39], v[38:39], v[134:135]
	v_pk_mul_f32 v[34:35], v[34:35], v[138:139]
	v_pk_mul_f32 v[32:33], v[32:33], v[128:129]
	v_pk_mul_f32 v[28:29], v[28:29], v[132:133]
	v_pk_mul_f32 v[24:25], v[24:25], v[136:137]
	v_pk_mul_f32 v[20:21], v[20:21], v[140:141]
	v_pk_mul_f32 v[30:31], v[30:31], v[126:127]
	v_pk_mul_f32 v[26:27], v[26:27], v[130:131]
	v_pk_mul_f32 v[22:23], v[22:23], v[134:135]
	v_pk_mul_f32 v[18:19], v[18:19], v[138:139]

; #define VMW() asm volatile("s_waitcnt vmcnt(0)" ::: "memory")
; #define SWRITE_H(bf) do { SWRITE_HV(bf); SWRITE_HK(bf); } while (0)
; template <int MODE>
; __device__ __forceinline__ void partialSM(f32x16& p0, f32x16& p1, float& m_reg, float& mn, float& alpha) {
;     constexpr float SCALE = Cfg<MODE>::SCALE;
;     float pmax = p0[0];
; #pragma unroll
;     for (int r = 1; r < 16; ++r) pmax = fmaxf(pmax, p0[r]);
; #pragma unroll
;     for (int r = 0; r < 16; ++r) pmax = fmaxf(pmax, p1[r]);
;     { auto rr = __builtin_amdgcn_permlane32_swap(__float_as_uint(pmax), __float_as_uint(pmax), false, false);
;       pmax = fmaxf(__uint_as_float(rr[0]), __uint_as_float(rr[1])); }
;     constexpr float C2 = 1.4426950408889634f * SCALE;
;     if (__builtin_expect(__all((pmax - m_reg) * SCALE <= THR), 1)) { mn = m_reg; alpha = 1.f; }
;     else { mn = fmaxf(m_reg, pmax); alpha = __builtin_amdgcn_exp2f((m_reg - mn) * C2); m_reg = mn; }
; template <int MODE>
; __device__ __forceinline__ void attn_block_pipe(const BlockRef& cur, const BlockRef& nxt, char* lds, LAS unsigned char* ldsl, Seam<MODE>& S) {
;     ...
;     MASKT(pA0, pA1, 0, 0); partialSM<MODE>(pA0, pA1, m_reg, mnA, alA);
;     if (NT > 1) { VMW(); SWRITE_H(1); }
.LBB0_731:
	v_max_f32_e32 v13, v50, v51
	v_max3_f32 v13, v13, v52, v53
	v_max3_f32 v13, v13, v54, v55
	v_max3_f32 v13, v13, v56, v57
	v_max3_f32 v13, v13, v58, v59
	v_max3_f32 v13, v13, v60, v61
	v_max3_f32 v13, v13, v62, v63
	v_max3_f32 v13, v13, v64, v65
	v_max3_f32 v13, v13, v34, v35
	v_max3_f32 v13, v13, v36, v37
	v_max3_f32 v13, v13, v38, v39
	v_max3_f32 v13, v13, v40, v41
	v_max3_f32 v13, v13, v42, v43
	v_max3_f32 v13, v13, v44, v45
	v_max3_f32 v13, v13, v46, v47
	v_max3_f32 v13, v13, v48, v49
	v_mov_b32_e32 v14, v13
	s_nop 1
	v_permlane32_swap_b32_e32 v13, v14
	v_max_f32_e32 v13, v13, v14
	v_add_f32_e32 v14, 0x7149f2ca, v13
	v_mul_f32_e32 v14, 0x3db504f3, v14
	v_cmp_ge_f32_e32 vcc, s78, v14
	s_cmp_eq_u64 vcc, exec
	s_cselect_b64 s[4:5], -1, 0
	s_andn2_b64 vcc, exec, s[6:7]
	s_cbranch_vccnz .LBB0_735
	s_waitcnt vmcnt(0)
	v_cmp_gt_i32_e32 vcc, 64, v213
	s_waitcnt vmcnt(0)
	ds_write_b128 v225, v[4:7] offset:16384
	ds_write_b128 v225, v[8:11] offset:24576
	s_and_saveexec_b64 s[6:7], vcc
	v_lshl_add_u32 v4, v213, 2, 0
	v_add_u32_e32 v4, 0x14900, v4
	ds_write_b32 v4, v207
	s_or_b64 exec, exec, s[6:7]

; template <int MODE>
; __device__ __forceinline__ void partialSM(f32x16& p0, f32x16& p1, float& m_reg, float& mn, float& alpha) {
;     constexpr float SCALE = Cfg<MODE>::SCALE;
;     float pmax = p0[0];
; #pragma unroll
;     for (int r = 1; r < 16; ++r) pmax = fmaxf(pmax, p0[r]);
; #pragma unroll
;     for (int r = 0; r < 16; ++r) pmax = fmaxf(pmax, p1[r]);
;     { auto rr = __builtin_amdgcn_permlane32_swap(__float_as_uint(pmax), __float_as_uint(pmax), false, false);
;       pmax = fmaxf(__uint_as_float(rr[0]), __uint_as_float(rr[1])); }
;     constexpr float C2 = 1.4426950408889634f * SCALE;
;     if (__builtin_expect(__all((pmax - m_reg) * SCALE <= THR), 1)) { mn = m_reg; alpha = 1.f; }
;     else { mn = fmaxf(m_reg, pmax); alpha = __builtin_amdgcn_exp2f((m_reg - mn) * C2); m_reg = mn; }
.LBB0_752:
	v_max_f32_e32 v12, v134, v135
	v_max3_f32 v12, v12, v136, v137
	v_max3_f32 v12, v12, v138, v139
	v_max3_f32 v12, v12, v140, v141
	v_max3_f32 v12, v12, v142, v143
	v_max3_f32 v12, v12, v144, v145
	v_max3_f32 v12, v12, v146, v147
	v_max3_f32 v12, v12, v148, v149
	v_max3_f32 v12, v12, v118, v119
	v_max3_f32 v12, v12, v120, v121
	v_max3_f32 v12, v12, v122, v123
	v_max3_f32 v12, v12, v124, v125
	v_max3_f32 v12, v12, v126, v127
	v_max3_f32 v12, v12, v128, v129
	v_max3_f32 v12, v12, v130, v131
	v_max3_f32 v12, v12, v132, v133
	v_mov_b32_e32 v13, v12
	s_nop 1
	v_permlane32_swap_b32_e32 v12, v13
	v_max_f32_e32 v12, v12, v13
	v_sub_f32_e32 v13, v12, v228
	v_mul_f32_e32 v13, 0x3db504f3, v13
	v_cmp_ge_f32_e32 vcc, s78, v13
	s_waitcnt vmcnt(0) lgkmcnt(0)
	s_barrier
	s_waitcnt vmcnt(0)
	s_cmp_eq_u64 vcc, exec
	s_cselect_b64 s[10:11], -1, 0
	ds_write_b128 v225, v[4:7]
	ds_write_b128 v225, v[8:11] offset:8192
	s_and_saveexec_b64 s[56:57], s[6:7]
	v_add_u32_e32 v13, 0, v230
	v_add_u32_e32 v13, 0x14800, v13
	ds_write_b32 v13, v207
	s_or_b64 exec, exec, s[56:57]
	v_max_f32_e32 v12, v228, v12
	v_sub_f32_e32 v13, v228, v12
	v_mul_f32_e32 v13, 0x3e0293ee, v13
	v_exp_f32_e32 v13, v13
	s_nop 0
	v_cndmask_b32_e64 v17, v13, 1.0, s[10:11]
	v_cmp_gt_f32_e32 vcc, 1.0, v17
	s_cbranch_vccz .LBB0_758
	s_and_saveexec_b64 s[56:57], s[4:5]
	ds_write_b32 v218, v17 offset:128
	s_or_b64 exec, exec, s[56:57]
	s_waitcnt lgkmcnt(0)
	ds_read_b128 v[20:23], v217 offset:224
	ds_read_b128 v[24:27], v217 offset:192
	ds_read_b128 v[28:31], v217 offset:160
	ds_read_b128 v[114:117], v217 offset:128
	s_waitcnt lgkmcnt(3)
	v_pk_mul_f32 v[96:97], v[96:97], v[22:23]
	s_waitcnt lgkmcnt(2)
	v_pk_mul_f32 v[92:93], v[92:93], v[26:27]
	s_waitcnt lgkmcnt(1)
	v_pk_mul_f32 v[88:89], v[88:89], v[30:31]
	s_waitcnt lgkmcnt(0)
	v_pk_mul_f32 v[84:85], v[84:85], v[116:117]
	v_pk_mul_f32 v[94:95], v[94:95], v[20:21]
	v_pk_mul_f32 v[90:91], v[90:91], v[24:25]
	v_pk_mul_f32 v[86:87], v[86:87], v[28:29]
	v_pk_mul_f32 v[82:83], v[82:83], v[114:115]
	v_pk_mul_f32 v[80:81], v[80:81], v[22:23]
	v_pk_mul_f32 v[76:77], v[76:77], v[26:27]
	v_pk_mul_f32 v[72:73], v[72:73], v[30:31]
	v_pk_mul_f32 v[68:69], v[68:69], v[116:117]
	v_pk_mul_f32 v[78:79], v[78:79], v[20:21]
	v_pk_mul_f32 v[74:75], v[74:75], v[24:25]
	v_pk_mul_f32 v[70:71], v[70:71], v[28:29]
	v_pk_mul_f32 v[66:67], v[66:67], v[114:115]
	v_pk_mul_f32 v[64:65], v[64:65], v[22:23]
	v_pk_mul_f32 v[60:61], v[60:61], v[26:27]
	v_pk_mul_f32 v[56:57], v[56:57], v[30:31]
	v_pk_mul_f32 v[52:53], v[52:53], v[116:117]
	v_pk_mul_f32 v[62:63], v[62:63], v[20:21]
	v_pk_mul_f32 v[58:59], v[58:59], v[24:25]
	v_pk_mul_f32 v[54:55], v[54:55], v[28:29]
	v_pk_mul_f32 v[50:51], v[50:51], v[114:115]
	v_pk_mul_f32 v[48:49], v[48:49], v[22:23]
	v_pk_mul_f32 v[44:45], v[44:45], v[26:27]
	v_pk_mul_f32 v[40:41], v[40:41], v[30:31]
	v_pk_mul_f32 v[36:37], v[36:37], v[116:117]
	v_pk_mul_f32 v[46:47], v[46:47], v[20:21]
	v_pk_mul_f32 v[42:43], v[42:43], v[24:25]
	v_pk_mul_f32 v[38:39], v[38:39], v[28:29]
	v_pk_mul_f32 v[34:35], v[34:35], v[114:115]

; template <int MODE>
; __device__ __forceinline__ void partialSM(f32x16& p0, f32x16& p1, float& m_reg, float& mn, float& alpha) {
;     constexpr float SCALE = Cfg<MODE>::SCALE;
;     float pmax = p0[0];
; #pragma unroll
;     for (int r = 1; r < 16; ++r) pmax = fmaxf(pmax, p0[r]);
; #pragma unroll
;     for (int r = 0; r < 16; ++r) pmax = fmaxf(pmax, p1[r]);
;     { auto rr = __builtin_amdgcn_permlane32_swap(__float_as_uint(pmax), __float_as_uint(pmax), false, false);
;       pmax = fmaxf(__uint_as_float(rr[0]), __uint_as_float(rr[1])); }
;     constexpr float C2 = 1.4426950408889634f * SCALE;
;     if (__builtin_expect(__all((pmax - m_reg) * SCALE <= THR), 1)) { mn = m_reg; alpha = 1.f; }
;     else { mn = fmaxf(m_reg, pmax); alpha = __builtin_amdgcn_exp2f((m_reg - mn) * C2); m_reg = mn; }
.LBB0_773:
	v_max_f32_e32 v12, v162, v163
	v_max3_f32 v12, v12, v164, v165
	v_max3_f32 v12, v12, v166, v167
	v_max3_f32 v12, v12, v168, v169
	v_max3_f32 v12, v12, v170, v171
	v_max3_f32 v12, v12, v172, v173
	v_max3_f32 v12, v12, v174, v175
	v_max3_f32 v12, v12, v176, v177
	v_max3_f32 v12, v12, v146, v147
	v_max3_f32 v12, v12, v148, v149
	v_max3_f32 v12, v12, v150, v151
	v_max3_f32 v12, v12, v152, v153
	v_max3_f32 v12, v12, v154, v155
	v_max3_f32 v12, v12, v156, v157
	v_max3_f32 v12, v12, v158, v159
	v_max3_f32 v12, v12, v160, v161
	v_mov_b32_e32 v13, v12
	s_nop 1
	v_permlane32_swap_b32_e32 v12, v13
	v_max_f32_e32 v12, v12, v13
	v_sub_f32_e32 v13, v12, v228
	v_mul_f32_e32 v13, 0x3db504f3, v13
	v_cmp_ge_f32_e32 vcc, s78, v13
	s_cmp_eq_u64 vcc, exec
	s_cselect_b64 s[8:9], -1, 0
	s_andn2_b64 vcc, exec, s[10:11]
	s_waitcnt vmcnt(0) lgkmcnt(0)
	s_barrier
	s_cbranch_vccnz .LBB0_777
	s_waitcnt vmcnt(0)
	ds_write_b128 v225, v[4:7] offset:16384
	ds_write_b128 v225, v[8:11] offset:24576
	s_and_saveexec_b64 s[10:11], s[6:7]
	v_add_u32_e32 v4, 0, v230
	v_add_u32_e32 v4, 0x14900, v4
	ds_write_b32 v4, v207
	s_or_b64 exec, exec, s[10:11]
.LBB0_777:
	v_max_f32_e32 v5, v228, v12
	v_sub_f32_e32 v4, v228, v5
	v_mul_f32_e32 v4, 0x3e0293ee, v4
	v_exp_f32_e32 v4, v4
	s_nop 0
	v_cndmask_b32_e64 v4, v4, 1.0, s[8:9]
	v_cmp_gt_f32_e32 vcc, 1.0, v4
	s_cbranch_vccz .LBB0_738
	s_and_saveexec_b64 s[10:11], s[4:5]
	s_cbranch_execz .LBB0_737
	ds_write_b32 v218, v4 offset:128
	s_branch .LBB0_737

; #define RESC(a) do { if (__any((a) < 1.f)) { if (hi == 0) al_l[r32] = (a); asm volatile("s_waitcnt lgkmcnt(0)" ::: "memory");              \
;                      _Pragma("unroll") for (int d_ = 0; d_ < 4; ++d_) _Pragma("unroll") for (int r = 0; r < 16; ++r) o[d_][r] *= al_l[crow(r, hi)]; } } while (0)
; #define RESC(a) do { if (__any((a) < 1.f)) { if (hi == 0) al_l[r32] = (a); asm volatile("s_waitcnt lgkmcnt(0)" ::: "memory");              \
;                      _Pragma("unroll") for (int d_ = 0; d_ < 4; ++d_) _Pragma("unroll") for (int r = 0; r < 16; ++r) o[d_][r] *= al_l[crow(r, hi)]; } } while (0)
; #define RESC(a) do { if (__any((a) < 1.f)) { if (hi == 0) al_l[r32] = (a); asm volatile("s_waitcnt lgkmcnt(0)" ::: "memory");              \
;                      _Pragma("unroll") for (int d_ = 0; d_ < 4; ++d_) _Pragma("unroll") for (int r = 0; r < 16; ++r) o[d_][r] *= al_l[crow(r, hi)]; } } while (0)
; template <int MODE>
; __device__ __forceinline__ void partialSM(f32x16& p0, f32x16& p1, float& m_reg, float& mn, float& alpha) {
;     constexpr float SCALE = Cfg<MODE>::SCALE;
;     float pmax = p0[0];
; #pragma unroll
;     for (int r = 1; r < 16; ++r) pmax = fmaxf(pmax, p0[r]);
; #pragma unroll
;     for (int r = 0; r < 16; ++r) pmax = fmaxf(pmax, p1[r]);
;     { auto rr = __builtin_amdgcn_permlane32_swap(__float_as_uint(pmax), __float_as_uint(pmax), false, false);
;       pmax = fmaxf(__uint_as_float(rr[0]), __uint_as_float(rr[1])); }
;     constexpr float C2 = 1.4426950408889634f * SCALE;
;     if (__builtin_expect(__all((pmax - m_reg) * SCALE <= THR), 1)) { mn = m_reg; alpha = 1.f; }
;     else { mn = fmaxf(m_reg, pmax); alpha = __builtin_amdgcn_exp2f((m_reg - mn) * C2); m_reg = mn; }
; template <int MODE>
; __device__ __forceinline__ void attn_block_pipe(const BlockRef& cur, const BlockRef& nxt, char* lds, LAS unsigned char* ldsl, Seam<MODE>& S) {
;     ...
;     if (even) { MASKT(pB0, pB1, NT - 1, 1); partialSM<MODE>(pB0, pB1, m_reg, mnB, alB); __syncthreads(); RESC(alB);
.LBB0_797:
	v_max_f32_e32 v2, v114, v115
	v_max3_f32 v2, v2, v116, v117
	v_max3_f32 v2, v2, v118, v119
	v_max3_f32 v2, v2, v120, v121
	v_max3_f32 v2, v2, v122, v123
	v_max3_f32 v2, v2, v124, v125
	v_max3_f32 v2, v2, v126, v127
	v_max3_f32 v2, v2, v128, v129
	v_max3_f32 v2, v2, v130, v131
	v_max3_f32 v2, v2, v132, v133
	v_max3_f32 v2, v2, v134, v135
	v_max3_f32 v2, v2, v136, v137
	v_max3_f32 v2, v2, v138, v139
	v_max3_f32 v2, v2, v140, v141
	v_max3_f32 v2, v2, v142, v143
	v_max3_f32 v2, v2, v144, v145
	v_mov_b32_e32 v16, v2
	s_nop 1
	v_permlane32_swap_b32_e32 v2, v16
	v_max_f32_e32 v2, v2, v16
	v_sub_f32_e32 v16, v2, v228
	v_mul_f32_e32 v17, 0x3db504f3, v16
	v_max_f32_e32 v16, v228, v2
	v_sub_f32_e32 v2, v228, v16
	v_mul_f32_e32 v2, 0x3e0293ee, v2
	v_exp_f32_e32 v2, v2
	v_cmp_ge_f32_e32 vcc, s78, v17
	s_cmp_eq_u64 vcc, exec
	s_cselect_b64 s[6:7], -1, 0
	v_cndmask_b32_e64 v2, v2, 1.0, s[6:7]
	v_cmp_gt_f32_e32 vcc, 1.0, v2
	s_waitcnt vmcnt(0) lgkmcnt(0)
	s_barrier
	s_cbranch_vccz .LBB0_801
	v_cmp_gt_u32_e32 vcc, 32, v215
	s_and_saveexec_b64 s[10:11], vcc
	ds_write_b32 v218, v2 offset:128
	s_or_b64 exec, exec, s[10:11]
	s_waitcnt lgkmcnt(0)
	ds_read_b128 v[98:101], v217 offset:224
	ds_read_b128 v[102:105], v217 offset:192
	ds_read_b128 v[106:109], v217 offset:160
	ds_read_b128 v[110:113], v217 offset:128
	s_waitcnt lgkmcnt(3)
	v_pk_mul_f32 v[96:97], v[96:97], v[100:101]
	s_waitcnt lgkmcnt(2)
	v_pk_mul_f32 v[92:93], v[92:93], v[104:105]
	s_waitcnt lgkmcnt(1)
	v_pk_mul_f32 v[88:89], v[88:89], v[108:109]
	s_waitcnt lgkmcnt(0)
	v_pk_mul_f32 v[84:85], v[84:85], v[112:113]
	v_pk_mul_f32 v[94:95], v[94:95], v[98:99]
	v_pk_mul_f32 v[90:91], v[90:91], v[102:103]
	v_pk_mul_f32 v[86:87], v[86:87], v[106:107]
	v_pk_mul_f32 v[82:83], v[82:83], v[110:111]
	v_pk_mul_f32 v[80:81], v[80:81], v[100:101]
	v_pk_mul_f32 v[76:77], v[76:77], v[104:105]
	v_pk_mul_f32 v[72:73], v[72:73], v[108:109]
	v_pk_mul_f32 v[68:69], v[68:69], v[112:113]
	v_pk_mul_f32 v[78:79], v[78:79], v[98:99]
	v_pk_mul_f32 v[74:75], v[74:75], v[102:103]
	v_pk_mul_f32 v[70:71], v[70:71], v[106:107]
	v_pk_mul_f32 v[66:67], v[66:67], v[110:111]
	v_pk_mul_f32 v[64:65], v[64:65], v[100:101]
	v_pk_mul_f32 v[60:61], v[60:61], v[104:105]
	v_pk_mul_f32 v[56:57], v[56:57], v[108:109]
	v_pk_mul_f32 v[52:53], v[52:53], v[112:113]
	v_pk_mul_f32 v[62:63], v[62:63], v[98:99]
	v_pk_mul_f32 v[58:59], v[58:59], v[102:103]
	v_pk_mul_f32 v[54:55], v[54:55], v[106:107]
	v_pk_mul_f32 v[50:51], v[50:51], v[110:111]
	v_pk_mul_f32 v[48:49], v[48:49], v[100:101]
	v_pk_mul_f32 v[44:45], v[44:45], v[104:105]
	v_pk_mul_f32 v[40:41], v[40:41], v[108:109]
	v_pk_mul_f32 v[36:37], v[36:37], v[112:113]
	v_pk_mul_f32 v[46:47], v[46:47], v[98:99]
	v_pk_mul_f32 v[42:43], v[42:43], v[102:103]
	v_pk_mul_f32 v[38:39], v[38:39], v[106:107]
	v_pk_mul_f32 v[34:35], v[34:35], v[110:111]

; #define VMW() asm volatile("s_waitcnt vmcnt(0)" ::: "memory")
; #define SWRITE_H(bf) do { SWRITE_HV(bf); SWRITE_HK(bf); } while (0)
; template <int MODE>
; __device__ __forceinline__ void partialSM(f32x16& p0, f32x16& p1, float& m_reg, float& mn, float& alpha) {
;     constexpr float SCALE = Cfg<MODE>::SCALE;
;     float pmax = p0[0];
; #pragma unroll
;     for (int r = 1; r < 16; ++r) pmax = fmaxf(pmax, p0[r]);
; #pragma unroll
;     for (int r = 0; r < 16; ++r) pmax = fmaxf(pmax, p1[r]);
;     { auto rr = __builtin_amdgcn_permlane32_swap(__float_as_uint(pmax), __float_as_uint(pmax), false, false);
;       pmax = fmaxf(__uint_as_float(rr[0]), __uint_as_float(rr[1])); }
;     constexpr float C2 = 1.4426950408889634f * SCALE;
;     if (__builtin_expect(__all((pmax - m_reg) * SCALE <= THR), 1)) { mn = m_reg; alpha = 1.f; }
;     else { mn = fmaxf(m_reg, pmax); alpha = __builtin_amdgcn_exp2f((m_reg - mn) * C2); m_reg = mn; }
; template <int MODE>
; __device__ __forceinline__ void attn_block_pipe(const BlockRef& cur, const BlockRef& nxt, char* lds, LAS unsigned char* ldsl, Seam<MODE>& S) {
;     ...
;     MASKT(pA0, pA1, 0, 0); partialSM<MODE>(pA0, pA1, m_reg, mnA, alA);
;     if (NT > 1) { VMW(); SWRITE_H(1); }
.LBB0_1030:
	s_nop 9
	v_max_f32_e32 v38, v20, v21
	v_max3_f32 v38, v38, v22, v23
	v_max3_f32 v38, v38, v24, v25
	v_max3_f32 v38, v38, v26, v27
	v_max3_f32 v38, v38, v28, v29
	v_max3_f32 v38, v38, v30, v31
	v_max3_f32 v38, v38, v32, v33
	v_max3_f32 v38, v38, v34, v35
	v_max3_f32 v38, v38, v4, v5
	v_max3_f32 v38, v38, v6, v7
	v_max3_f32 v38, v38, v8, v9
	v_max3_f32 v38, v38, v10, v11
	v_max3_f32 v38, v38, v12, v13
	v_max3_f32 v38, v38, v14, v15
	v_max3_f32 v38, v38, v16, v17
	v_max3_f32 v38, v38, v18, v19
	v_mov_b32_e32 v39, v38
	s_nop 1
	v_permlane32_swap_b32_e32 v38, v39
	v_max_f32_e32 v38, v38, v39
	v_add_f32_e32 v39, 0x7149f2ca, v38
	v_mul_f32_e32 v39, 0x3d93cd3a, v39
	v_cmp_ge_f32_e32 vcc, s56, v39
	s_cmp_eq_u64 vcc, exec
	s_cselect_b64 s[4:5], -1, 0
	s_andn2_b64 vcc, exec, s[44:45]
	s_cbranch_vccnz .LBB0_1032
	s_waitcnt vmcnt(0)
	s_waitcnt vmcnt(0)
	ds_write_b128 v2, v[114:117] offset:16384
	ds_write_b128 v2, v[118:121] offset:24576

; template <int MODE>
; __device__ __forceinline__ void partialSM(f32x16& p0, f32x16& p1, float& m_reg, float& mn, float& alpha) {
;     constexpr float SCALE = Cfg<MODE>::SCALE;
;     float pmax = p0[0];
; #pragma unroll
;     for (int r = 1; r < 16; ++r) pmax = fmaxf(pmax, p0[r]);
; #pragma unroll
;     for (int r = 0; r < 16; ++r) pmax = fmaxf(pmax, p1[r]);
;     { auto rr = __builtin_amdgcn_permlane32_swap(__float_as_uint(pmax), __float_as_uint(pmax), false, false);
;       pmax = fmaxf(__uint_as_float(rr[0]), __uint_as_float(rr[1])); }
;     constexpr float C2 = 1.4426950408889634f * SCALE;
;     if (__builtin_expect(__all((pmax - m_reg) * SCALE <= THR), 1)) { mn = m_reg; alpha = 1.f; }
;     else { mn = fmaxf(m_reg, pmax); alpha = __builtin_amdgcn_exp2f((m_reg - mn) * C2); m_reg = mn; }
.LBB0_1038:
	v_max_f32_e32 v12, v102, v103
	v_max3_f32 v12, v12, v104, v105
	v_max3_f32 v12, v12, v106, v107
	v_max3_f32 v12, v12, v108, v109
	v_max3_f32 v12, v12, v110, v111
	v_max3_f32 v12, v12, v112, v113
	v_max3_f32 v12, v12, v114, v115
	v_max3_f32 v12, v12, v116, v117
	v_max3_f32 v12, v12, v86, v87
	v_max3_f32 v12, v12, v88, v89
	v_max3_f32 v12, v12, v90, v91
	v_max3_f32 v12, v12, v92, v93
	v_max3_f32 v12, v12, v94, v95
	v_max3_f32 v12, v12, v96, v97
	v_max3_f32 v12, v12, v98, v99
	v_max3_f32 v12, v12, v100, v101
	v_mov_b32_e32 v13, v12
	s_nop 1
	v_permlane32_swap_b32_e32 v12, v13
	v_max_f32_e32 v12, v12, v13
	v_sub_f32_e32 v13, v12, v178
	v_max_f32_e32 v12, v178, v12
	v_sub_f32_e32 v14, v178, v12
	v_mul_f32_e32 v14, 0x3dd53b94, v14
	v_mul_f32_e32 v13, 0x3d93cd3a, v13
	v_exp_f32_e32 v14, v14
	v_cmp_ge_f32_e32 vcc, s56, v13
	s_cmp_eq_u64 vcc, exec
	s_cselect_b64 s[6:7], -1, 0
	s_waitcnt vmcnt(0) lgkmcnt(0)
	s_barrier
	s_waitcnt vmcnt(0)
	v_cndmask_b32_e64 v226, v14, 1.0, s[6:7]
	v_cmp_gt_f32_e32 vcc, 1.0, v226
	ds_write_b128 v2, v[4:7]
	ds_write_b128 v2, v[8:11] offset:8192
	s_cbranch_vccz .LBB0_1042
	s_and_saveexec_b64 s[44:45], s[4:5]
	ds_write_b32 v208, v226 offset:128
	s_or_b64 exec, exec, s[44:45]
	s_waitcnt lgkmcnt(0)
	ds_read_b128 v[82:85], v207 offset:224
	ds_read_b128 v[118:121], v207 offset:192
	ds_read_b128 v[122:125], v207 offset:160
	ds_read_b128 v[126:129], v207 offset:128
	s_waitcnt lgkmcnt(3)
	v_pk_mul_f32 v[80:81], v[80:81], v[84:85]
	s_waitcnt lgkmcnt(2)
	v_pk_mul_f32 v[76:77], v[76:77], v[120:121]
	s_waitcnt lgkmcnt(1)
	v_pk_mul_f32 v[72:73], v[72:73], v[124:125]
	s_waitcnt lgkmcnt(0)
	v_pk_mul_f32 v[68:69], v[68:69], v[128:129]
	v_pk_mul_f32 v[78:79], v[78:79], v[82:83]
	v_pk_mul_f32 v[74:75], v[74:75], v[118:119]
	v_pk_mul_f32 v[70:71], v[70:71], v[122:123]
	v_pk_mul_f32 v[66:67], v[66:67], v[126:127]
	v_pk_mul_f32 v[64:65], v[64:65], v[84:85]
	v_pk_mul_f32 v[60:61], v[60:61], v[120:121]
	v_pk_mul_f32 v[56:57], v[56:57], v[124:125]
	v_pk_mul_f32 v[52:53], v[52:53], v[128:129]
	v_pk_mul_f32 v[62:63], v[62:63], v[82:83]
	v_pk_mul_f32 v[58:59], v[58:59], v[118:119]
	v_pk_mul_f32 v[54:55], v[54:55], v[122:123]
	v_pk_mul_f32 v[50:51], v[50:51], v[126:127]
	v_pk_mul_f32 v[48:49], v[48:49], v[84:85]
	v_pk_mul_f32 v[44:45], v[44:45], v[120:121]
	v_pk_mul_f32 v[40:41], v[40:41], v[124:125]
	v_pk_mul_f32 v[36:37], v[36:37], v[128:129]
	v_pk_mul_f32 v[46:47], v[46:47], v[82:83]
	v_pk_mul_f32 v[42:43], v[42:43], v[118:119]
	v_pk_mul_f32 v[38:39], v[38:39], v[122:123]
	v_pk_mul_f32 v[34:35], v[34:35], v[126:127]
	v_pk_mul_f32 v[32:33], v[32:33], v[84:85]
	v_pk_mul_f32 v[28:29], v[28:29], v[120:121]
	v_pk_mul_f32 v[24:25], v[24:25], v[124:125]
	v_pk_mul_f32 v[20:21], v[20:21], v[128:129]
	v_pk_mul_f32 v[30:31], v[30:31], v[82:83]
	v_pk_mul_f32 v[26:27], v[26:27], v[118:119]
	v_pk_mul_f32 v[22:23], v[22:23], v[122:123]
	v_pk_mul_f32 v[18:19], v[18:19], v[126:127]

; template <int MODE>
; __device__ __forceinline__ void partialSM(f32x16& p0, f32x16& p1, float& m_reg, float& mn, float& alpha) {
;     constexpr float SCALE = Cfg<MODE>::SCALE;
;     float pmax = p0[0];
; #pragma unroll
;     for (int r = 1; r < 16; ++r) pmax = fmaxf(pmax, p0[r]);
; #pragma unroll
;     for (int r = 0; r < 16; ++r) pmax = fmaxf(pmax, p1[r]);
;     { auto rr = __builtin_amdgcn_permlane32_swap(__float_as_uint(pmax), __float_as_uint(pmax), false, false);
;       pmax = fmaxf(__uint_as_float(rr[0]), __uint_as_float(rr[1])); }
;     constexpr float C2 = 1.4426950408889634f * SCALE;
;     if (__builtin_expect(__all((pmax - m_reg) * SCALE <= THR), 1)) { mn = m_reg; alpha = 1.f; }
;     else { mn = fmaxf(m_reg, pmax); alpha = __builtin_amdgcn_exp2f((m_reg - mn) * C2); m_reg = mn; }
.LBB0_1046:
	v_max_f32_e32 v12, v130, v131
	v_max3_f32 v12, v12, v132, v133
	v_max3_f32 v12, v12, v134, v135
	v_max3_f32 v12, v12, v136, v137
	v_max3_f32 v12, v12, v138, v139
	v_max3_f32 v12, v12, v140, v141
	v_max3_f32 v12, v12, v142, v143
	v_max3_f32 v12, v12, v144, v145
	v_max3_f32 v12, v12, v114, v115
	v_max3_f32 v12, v12, v116, v117
	v_max3_f32 v12, v12, v118, v119
	v_max3_f32 v12, v12, v120, v121
	v_max3_f32 v12, v12, v122, v123
	v_max3_f32 v12, v12, v124, v125
	v_max3_f32 v12, v12, v126, v127
	v_max3_f32 v12, v12, v128, v129
	v_mov_b32_e32 v13, v12
	s_nop 1
	v_permlane32_swap_b32_e32 v12, v13
	v_max_f32_e32 v12, v12, v13
	v_sub_f32_e32 v13, v12, v227
	v_mul_f32_e32 v13, 0x3d93cd3a, v13
	v_cmp_ge_f32_e32 vcc, s56, v13
	s_cmp_eq_u64 vcc, exec
	s_cselect_b64 s[6:7], -1, 0
	s_andn2_b64 vcc, exec, s[44:45]
	s_waitcnt vmcnt(0) lgkmcnt(0)
	s_barrier
	s_cbranch_vccnz .LBB0_1048
	s_waitcnt vmcnt(0)
	ds_write_b128 v2, v[4:7] offset:16384
	ds_write_b128 v2, v[8:11] offset:24576
.LBB0_1048:
	v_max_f32_e32 v5, v227, v12
	v_sub_f32_e32 v4, v227, v5
	v_mul_f32_e32 v4, 0x3dd53b94, v4
	v_exp_f32_e32 v4, v4
	s_nop 0
	v_cndmask_b32_e64 v4, v4, 1.0, s[6:7]
	v_cmp_gt_f32_e32 vcc, 1.0, v4
	s_cbranch_vccz .LBB0_1035
	s_and_saveexec_b64 s[44:45], s[4:5]
	s_cbranch_execz .LBB0_1034
	ds_write_b32 v208, v4 offset:128
	s_branch .LBB0_1034

; #define RESC(a) do { if (__any((a) < 1.f)) { if (hi == 0) al_l[r32] = (a); asm volatile("s_waitcnt lgkmcnt(0)" ::: "memory");              \
;                      _Pragma("unroll") for (int d_ = 0; d_ < 4; ++d_) _Pragma("unroll") for (int r = 0; r < 16; ++r) o[d_][r] *= al_l[crow(r, hi)]; } } while (0)
; #define RESC(a) do { if (__any((a) < 1.f)) { if (hi == 0) al_l[r32] = (a); asm volatile("s_waitcnt lgkmcnt(0)" ::: "memory");              \
;                      _Pragma("unroll") for (int d_ = 0; d_ < 4; ++d_) _Pragma("unroll") for (int r = 0; r < 16; ++r) o[d_][r] *= al_l[crow(r, hi)]; } } while (0)
; #define RESC(a) do { if (__any((a) < 1.f)) { if (hi == 0) al_l[r32] = (a); asm volatile("s_waitcnt lgkmcnt(0)" ::: "memory");              \
;                      _Pragma("unroll") for (int d_ = 0; d_ < 4; ++d_) _Pragma("unroll") for (int r = 0; r < 16; ++r) o[d_][r] *= al_l[crow(r, hi)]; } } while (0)
; template <int MODE>
; __device__ __forceinline__ void partialSM(f32x16& p0, f32x16& p1, float& m_reg, float& mn, float& alpha) {
;     constexpr float SCALE = Cfg<MODE>::SCALE;
;     float pmax = p0[0];
; #pragma unroll
;     for (int r = 1; r < 16; ++r) pmax = fmaxf(pmax, p0[r]);
; #pragma unroll
;     for (int r = 0; r < 16; ++r) pmax = fmaxf(pmax, p1[r]);
;     { auto rr = __builtin_amdgcn_permlane32_swap(__float_as_uint(pmax), __float_as_uint(pmax), false, false);
;       pmax = fmaxf(__uint_as_float(rr[0]), __uint_as_float(rr[1])); }
;     constexpr float C2 = 1.4426950408889634f * SCALE;
;     if (__builtin_expect(__all((pmax - m_reg) * SCALE <= THR), 1)) { mn = m_reg; alpha = 1.f; }
;     else { mn = fmaxf(m_reg, pmax); alpha = __builtin_amdgcn_exp2f((m_reg - mn) * C2); m_reg = mn; }
; template <int MODE>
; __device__ __forceinline__ void attn_block_pipe(const BlockRef& cur, const BlockRef& nxt, char* lds, LAS unsigned char* ldsl, Seam<MODE>& S) {
;     ...
;     if (even) { MASKT(pB0, pB1, NT - 1, 1); partialSM<MODE>(pB0, pB1, m_reg, mnB, alB); __syncthreads(); RESC(alB);
.LBB0_1057:
	v_max_f32_e32 v16, v82, v83
	v_max3_f32 v16, v16, v84, v85
	v_max3_f32 v16, v16, v86, v87
	v_max3_f32 v16, v16, v88, v89
	v_max3_f32 v16, v16, v90, v91
	v_max3_f32 v16, v16, v92, v93
	v_max3_f32 v16, v16, v94, v95
	v_max3_f32 v16, v16, v96, v97
	v_max3_f32 v16, v16, v98, v99
	v_max3_f32 v16, v16, v100, v101
	v_max3_f32 v16, v16, v102, v103
	v_max3_f32 v16, v16, v104, v105
	v_max3_f32 v16, v16, v106, v107
	v_max3_f32 v16, v16, v108, v109
	v_max3_f32 v16, v16, v110, v111
	v_max3_f32 v16, v16, v112, v113
	v_mov_b32_e32 v17, v16
	s_nop 1
	v_permlane32_swap_b32_e32 v16, v17
	v_max_f32_e32 v16, v16, v17
	v_sub_f32_e32 v17, v16, v178
	v_mul_f32_e32 v126, 0x3d93cd3a, v17
	v_max_f32_e32 v17, v178, v16
	v_sub_f32_e32 v16, v178, v17
	v_mul_f32_e32 v16, 0x3dd53b94, v16
	v_exp_f32_e32 v16, v16
	v_cmp_ge_f32_e32 vcc, s56, v126
	s_cmp_eq_u64 vcc, exec
	s_cselect_b64 s[4:5], -1, 0
	v_cndmask_b32_e64 v16, v16, 1.0, s[4:5]
	v_cmp_gt_f32_e32 vcc, 1.0, v16
	s_waitcnt vmcnt(0) lgkmcnt(0)
	s_barrier
	s_cbranch_vccz .LBB0_1061
	v_cmp_gt_u32_e32 vcc, 32, v206
	s_and_saveexec_b64 s[6:7], vcc
	ds_write_b32 v208, v16 offset:128
	s_or_b64 exec, exec, s[6:7]
	s_waitcnt lgkmcnt(0)
	ds_read_b128 v[126:129], v207 offset:224
	ds_read_b128 v[130:133], v207 offset:192
	ds_read_b128 v[134:137], v207 offset:160
	ds_read_b128 v[138:141], v207 offset:128
	s_waitcnt lgkmcnt(3)
	v_pk_mul_f32 v[80:81], v[80:81], v[128:129]
	s_waitcnt lgkmcnt(2)
	v_pk_mul_f32 v[76:77], v[76:77], v[132:133]
	s_waitcnt lgkmcnt(1)
	v_pk_mul_f32 v[72:73], v[72:73], v[136:137]
	s_waitcnt lgkmcnt(0)
	v_pk_mul_f32 v[68:69], v[68:69], v[140:141]
	v_pk_mul_f32 v[78:79], v[78:79], v[126:127]
	v_pk_mul_f32 v[74:75], v[74:75], v[130:131]
	v_pk_mul_f32 v[70:71], v[70:71], v[134:135]
	v_pk_mul_f32 v[66:67], v[66:67], v[138:139]
	v_pk_mul_f32 v[64:65], v[64:65], v[128:129]
	v_pk_mul_f32 v[60:61], v[60:61], v[132:133]
	v_pk_mul_f32 v[56:57], v[56:57], v[136:137]
	v_pk_mul_f32 v[52:53], v[52:53], v[140:141]
	v_pk_mul_f32 v[62:63], v[62:63], v[126:127]
	v_pk_mul_f32 v[58:59], v[58:59], v[130:131]
	v_pk_mul_f32 v[54:55], v[54:55], v[134:135]
	v_pk_mul_f32 v[50:51], v[50:51], v[138:139]
	v_pk_mul_f32 v[48:49], v[48:49], v[128:129]
	v_pk_mul_f32 v[44:45], v[44:45], v[132:133]
	v_pk_mul_f32 v[40:41], v[40:41], v[136:137]
	v_pk_mul_f32 v[36:37], v[36:37], v[140:141]
	v_pk_mul_f32 v[46:47], v[46:47], v[126:127]
	v_pk_mul_f32 v[42:43], v[42:43], v[130:131]
	v_pk_mul_f32 v[38:39], v[38:39], v[134:135]
	v_pk_mul_f32 v[34:35], v[34:35], v[138:139]
	v_pk_mul_f32 v[32:33], v[32:33], v[128:129]
	v_pk_mul_f32 v[28:29], v[28:29], v[132:133]
	v_pk_mul_f32 v[24:25], v[24:25], v[136:137]
	v_pk_mul_f32 v[20:21], v[20:21], v[140:141]
	v_pk_mul_f32 v[30:31], v[30:31], v[126:127]
	v_pk_mul_f32 v[26:27], v[26:27], v[130:131]
	v_pk_mul_f32 v[22:23], v[22:23], v[134:135]
	v_pk_mul_f32 v[18:19], v[18:19], v[138:139]
